# P8 epilogue wide stores regrouped so each row gets 32 contiguous bytes per store instruction (tiles m,m+1 x n0,n1)
# speedup vs baseline: 1.0222x; 1.0063x over previous
.LBB0_1047:
	s_ashr_i32 s7, s6, 31
	s_lshl_b64 s[26:27], s[6:7], 13
	s_add_u32 s7, s86, s26
	s_addc_u32 s28, s87, s27
	s_ashr_i32 s11, s10, 31
	s_lshl_b64 s[26:27], s[10:11], 2
	s_add_u32 s7, s7, s26
	s_addc_u32 s27, s28, s27
	s_add_u32 s26, s7, s72
	s_addc_u32 s27, s27, 0
	global_load_dwordx4 v[12:15], v198, s[26:27]
	global_load_dwordx4 v[8:11], v198, s[26:27] offset:64
	global_load_dwordx4 v[4:7], v198, s[26:27] offset:512
	global_load_dwordx4 v[0:3], v198, s[26:27] offset:576
	s_andn2_b64 vcc, exec, s[24:25]
	v_bfe_u32 v251, v178, 4, 1
	v_lshl_add_u32 v16, v251, 4, v193
	v_add_u32_e32 v16, s44, v16
	s_mov_b64 s[100:101], 0x10000
	v_ashrrev_i32_e32 v17, 31, v16
	v_lshlrev_b64 v[252:253], 11, v[16:17]
	v_bfe_u32 v16, v178, 5, 1
	v_lshlrev_b32_e32 v16, 4, v16
	v_mov_b32_e32 v17, 0
	v_lshl_add_u64 v[252:253], s[16:17], 0, v[252:253]
	v_lshl_add_u64 v[252:253], v[252:253], 0, s[10:11]
	v_lshl_add_u64 v[252:253], v[252:253], 0, s[14:15]
	v_lshl_add_u64 v[252:253], v[252:253], 0, v[16:17]
	v_lshl_add_u64 v[254:255], v[252:253], 0, s[100:101]
	s_mov_b64 s[100:101], 0x40000
	v_lshl_add_u64 v[226:227], v[252:253], 0, s[100:101]
	v_lshl_add_u64 v[228:229], v[254:255], 0, s[100:101]
	s_waitcnt vmcnt(0)
	v_pk_add_f32 v[24:25], v[172:173], v[12:13]
	v_pk_add_f32 v[26:27], v[174:175], v[14:15]
	v_pk_add_f32 v[28:29], v[164:165], v[12:13]
	v_pk_add_f32 v[30:31], v[166:167], v[14:15]
	v_pk_add_f32 v[32:33], v[168:169], v[8:9]
	v_pk_add_f32 v[34:35], v[170:171], v[10:11]
	v_pk_add_f32 v[36:37], v[160:161], v[8:9]
	v_pk_add_f32 v[38:39], v[162:163], v[10:11]
	v_med3_f32 v24, v24, s77, v200
	v_med3_f32 v25, v25, s77, v200
	v_med3_f32 v26, v26, s77, v200
	v_med3_f32 v27, v27, s77, v200
	v_med3_f32 v28, v28, s77, v200
	v_med3_f32 v29, v29, s77, v200
	v_med3_f32 v30, v30, s77, v200
	v_med3_f32 v31, v31, s77, v200
	v_med3_f32 v32, v32, s77, v200
	v_med3_f32 v33, v33, s77, v200
	v_med3_f32 v34, v34, s77, v200
	v_med3_f32 v35, v35, s77, v200
	v_med3_f32 v36, v36, s77, v200
	v_med3_f32 v37, v37, s77, v200
	v_med3_f32 v38, v38, s77, v200
	v_med3_f32 v39, v39, s77, v200
	v_cvt_pk_fp8_f32 v20, v24, v25
	v_cvt_pk_fp8_f32 v21, v28, v29
	v_cvt_pk_fp8_f32 v22, v32, v33
	v_cvt_pk_fp8_f32 v23, v36, v37
	v_cvt_pk_fp8_f32 v20, v26, v27 op_sel:[0,0,1]
	v_cvt_pk_fp8_f32 v21, v30, v31 op_sel:[0,0,1]
	v_cvt_pk_fp8_f32 v22, v34, v35 op_sel:[0,0,1]
	v_cvt_pk_fp8_f32 v23, v38, v39 op_sel:[0,0,1]
	s_nop 1
	v_permlane32_swap_b32_e32 v20, v22
	v_permlane32_swap_b32_e32 v21, v23
	s_nop 1
	v_permlane16_swap_b32_e32 v20, v21
	v_permlane16_swap_b32_e32 v22, v23
	global_store_dwordx4 v[252:253], v[20:23], off
	v_pk_add_f32 v[24:25], v[156:157], v[12:13]
	v_pk_add_f32 v[26:27], v[158:159], v[14:15]
	v_pk_add_f32 v[28:29], v[148:149], v[12:13]
	v_pk_add_f32 v[30:31], v[150:151], v[14:15]
	v_pk_add_f32 v[32:33], v[152:153], v[8:9]
	v_pk_add_f32 v[34:35], v[154:155], v[10:11]
	v_pk_add_f32 v[36:37], v[144:145], v[8:9]
	v_pk_add_f32 v[38:39], v[146:147], v[10:11]
	v_med3_f32 v24, v24, s77, v200
	v_med3_f32 v25, v25, s77, v200
	v_med3_f32 v26, v26, s77, v200
	v_med3_f32 v27, v27, s77, v200
	v_med3_f32 v28, v28, s77, v200
	v_med3_f32 v29, v29, s77, v200
	v_med3_f32 v30, v30, s77, v200
	v_med3_f32 v31, v31, s77, v200
	v_med3_f32 v32, v32, s77, v200
	v_med3_f32 v33, v33, s77, v200
	v_med3_f32 v34, v34, s77, v200
	v_med3_f32 v35, v35, s77, v200
	v_med3_f32 v36, v36, s77, v200
	v_med3_f32 v37, v37, s77, v200
	v_med3_f32 v38, v38, s77, v200
	v_med3_f32 v39, v39, s77, v200
	v_cvt_pk_fp8_f32 v40, v24, v25
	v_cvt_pk_fp8_f32 v41, v28, v29
	v_cvt_pk_fp8_f32 v42, v32, v33
	v_cvt_pk_fp8_f32 v43, v36, v37
	v_cvt_pk_fp8_f32 v40, v26, v27 op_sel:[0,0,1]
	v_cvt_pk_fp8_f32 v41, v30, v31 op_sel:[0,0,1]
	v_cvt_pk_fp8_f32 v42, v34, v35 op_sel:[0,0,1]
	v_cvt_pk_fp8_f32 v43, v38, v39 op_sel:[0,0,1]
	s_nop 1
	v_permlane32_swap_b32_e32 v40, v42
	v_permlane32_swap_b32_e32 v41, v43
	s_nop 1
	v_permlane16_swap_b32_e32 v40, v41
	v_permlane16_swap_b32_e32 v42, v43
	global_store_dwordx4 v[254:255], v[40:43], off
	v_pk_add_f32 v[24:25], v[140:141], v[4:5]
	v_pk_add_f32 v[26:27], v[142:143], v[6:7]
	v_pk_add_f32 v[28:29], v[132:133], v[4:5]
	v_pk_add_f32 v[30:31], v[134:135], v[6:7]
	v_pk_add_f32 v[32:33], v[136:137], v[0:1]
	v_pk_add_f32 v[34:35], v[138:139], v[2:3]
	v_pk_add_f32 v[36:37], v[128:129], v[0:1]
	v_pk_add_f32 v[38:39], v[130:131], v[2:3]
	v_med3_f32 v24, v24, s77, v200
	v_med3_f32 v25, v25, s77, v200
	v_med3_f32 v26, v26, s77, v200
	v_med3_f32 v27, v27, s77, v200
	v_med3_f32 v28, v28, s77, v200
	v_med3_f32 v29, v29, s77, v200
	v_med3_f32 v30, v30, s77, v200
	v_med3_f32 v31, v31, s77, v200
	v_med3_f32 v32, v32, s77, v200
	v_med3_f32 v33, v33, s77, v200
	v_med3_f32 v34, v34, s77, v200
	v_med3_f32 v35, v35, s77, v200
	v_med3_f32 v36, v36, s77, v200
	v_med3_f32 v37, v37, s77, v200
	v_med3_f32 v38, v38, s77, v200
	v_med3_f32 v39, v39, s77, v200
	v_cvt_pk_fp8_f32 v20, v24, v25
	v_cvt_pk_fp8_f32 v21, v28, v29
	v_cvt_pk_fp8_f32 v22, v32, v33
	v_cvt_pk_fp8_f32 v23, v36, v37
	v_cvt_pk_fp8_f32 v20, v26, v27 op_sel:[0,0,1]
	v_cvt_pk_fp8_f32 v21, v30, v31 op_sel:[0,0,1]
	v_cvt_pk_fp8_f32 v22, v34, v35 op_sel:[0,0,1]
	v_cvt_pk_fp8_f32 v23, v38, v39 op_sel:[0,0,1]
	s_nop 1
	v_permlane32_swap_b32_e32 v20, v22
	v_permlane32_swap_b32_e32 v21, v23
	s_nop 1
	v_permlane16_swap_b32_e32 v20, v21
	v_permlane16_swap_b32_e32 v22, v23
	global_store_dwordx4 v[252:253], v[20:23], off offset:128
	v_pk_add_f32 v[24:25], v[124:125], v[4:5]
	v_pk_add_f32 v[26:27], v[126:127], v[6:7]
	v_pk_add_f32 v[28:29], v[116:117], v[4:5]
	v_pk_add_f32 v[30:31], v[118:119], v[6:7]
	v_pk_add_f32 v[32:33], v[120:121], v[0:1]
	v_pk_add_f32 v[34:35], v[122:123], v[2:3]
	v_pk_add_f32 v[36:37], v[112:113], v[0:1]
	v_pk_add_f32 v[38:39], v[114:115], v[2:3]
	v_med3_f32 v24, v24, s77, v200
	v_med3_f32 v25, v25, s77, v200
	v_med3_f32 v26, v26, s77, v200
	v_med3_f32 v27, v27, s77, v200
	v_med3_f32 v28, v28, s77, v200
	v_med3_f32 v29, v29, s77, v200
	v_med3_f32 v30, v30, s77, v200
	v_med3_f32 v31, v31, s77, v200
	v_med3_f32 v32, v32, s77, v200
	v_med3_f32 v33, v33, s77, v200
	v_med3_f32 v34, v34, s77, v200
	v_med3_f32 v35, v35, s77, v200
	v_med3_f32 v36, v36, s77, v200
	v_med3_f32 v37, v37, s77, v200
	v_med3_f32 v38, v38, s77, v200
	v_med3_f32 v39, v39, s77, v200
	v_cvt_pk_fp8_f32 v40, v24, v25
	v_cvt_pk_fp8_f32 v41, v28, v29
	v_cvt_pk_fp8_f32 v42, v32, v33
	v_cvt_pk_fp8_f32 v43, v36, v37
	v_cvt_pk_fp8_f32 v40, v26, v27 op_sel:[0,0,1]
	v_cvt_pk_fp8_f32 v41, v30, v31 op_sel:[0,0,1]
	v_cvt_pk_fp8_f32 v42, v34, v35 op_sel:[0,0,1]
	v_cvt_pk_fp8_f32 v43, v38, v39 op_sel:[0,0,1]
	s_nop 1
	v_permlane32_swap_b32_e32 v40, v42
	v_permlane32_swap_b32_e32 v41, v43
	s_nop 1
	v_permlane16_swap_b32_e32 v40, v41
	v_permlane16_swap_b32_e32 v42, v43
	global_store_dwordx4 v[254:255], v[40:43], off offset:128
	v_pk_add_f32 v[24:25], v[108:109], v[12:13]
	v_pk_add_f32 v[26:27], v[110:111], v[14:15]
	v_pk_add_f32 v[28:29], v[100:101], v[12:13]
	v_pk_add_f32 v[30:31], v[102:103], v[14:15]
	v_pk_add_f32 v[32:33], v[104:105], v[8:9]
	v_pk_add_f32 v[34:35], v[106:107], v[10:11]
	v_pk_add_f32 v[36:37], v[96:97], v[8:9]
	v_pk_add_f32 v[38:39], v[98:99], v[10:11]
	v_med3_f32 v24, v24, s77, v200
	v_med3_f32 v25, v25, s77, v200
	v_med3_f32 v26, v26, s77, v200
	v_med3_f32 v27, v27, s77, v200
	v_med3_f32 v28, v28, s77, v200
	v_med3_f32 v29, v29, s77, v200
	v_med3_f32 v30, v30, s77, v200
	v_med3_f32 v31, v31, s77, v200
	v_med3_f32 v32, v32, s77, v200
	v_med3_f32 v33, v33, s77, v200
	v_med3_f32 v34, v34, s77, v200
	v_med3_f32 v35, v35, s77, v200
	v_med3_f32 v36, v36, s77, v200
	v_med3_f32 v37, v37, s77, v200
	v_med3_f32 v38, v38, s77, v200
	v_med3_f32 v39, v39, s77, v200
	v_cvt_pk_fp8_f32 v20, v24, v25
	v_cvt_pk_fp8_f32 v21, v28, v29
	v_cvt_pk_fp8_f32 v22, v32, v33
	v_cvt_pk_fp8_f32 v23, v36, v37
	v_cvt_pk_fp8_f32 v20, v26, v27 op_sel:[0,0,1]
	v_cvt_pk_fp8_f32 v21, v30, v31 op_sel:[0,0,1]
	v_cvt_pk_fp8_f32 v22, v34, v35 op_sel:[0,0,1]
	v_cvt_pk_fp8_f32 v23, v38, v39 op_sel:[0,0,1]
	s_nop 1
	v_permlane32_swap_b32_e32 v20, v22
	v_permlane32_swap_b32_e32 v21, v23
	s_nop 1
	v_permlane16_swap_b32_e32 v20, v21
	v_permlane16_swap_b32_e32 v22, v23
	global_store_dwordx4 v[226:227], v[20:23], off
	v_pk_add_f32 v[24:25], v[92:93], v[12:13]
	v_pk_add_f32 v[26:27], v[94:95], v[14:15]
	v_pk_add_f32 v[28:29], v[84:85], v[12:13]
	v_pk_add_f32 v[30:31], v[86:87], v[14:15]
	v_pk_add_f32 v[32:33], v[88:89], v[8:9]
	v_pk_add_f32 v[34:35], v[90:91], v[10:11]
	v_pk_add_f32 v[36:37], v[80:81], v[8:9]
	v_pk_add_f32 v[38:39], v[82:83], v[10:11]
	v_med3_f32 v24, v24, s77, v200
	v_med3_f32 v25, v25, s77, v200
	v_med3_f32 v26, v26, s77, v200
	v_med3_f32 v27, v27, s77, v200
	v_med3_f32 v28, v28, s77, v200
	v_med3_f32 v29, v29, s77, v200
	v_med3_f32 v30, v30, s77, v200
	v_med3_f32 v31, v31, s77, v200
	v_med3_f32 v32, v32, s77, v200
	v_med3_f32 v33, v33, s77, v200
	v_med3_f32 v34, v34, s77, v200
	v_med3_f32 v35, v35, s77, v200
	v_med3_f32 v36, v36, s77, v200
	v_med3_f32 v37, v37, s77, v200
	v_med3_f32 v38, v38, s77, v200
	v_med3_f32 v39, v39, s77, v200
	v_cvt_pk_fp8_f32 v40, v24, v25
	v_cvt_pk_fp8_f32 v41, v28, v29
	v_cvt_pk_fp8_f32 v42, v32, v33
	v_cvt_pk_fp8_f32 v43, v36, v37
	v_cvt_pk_fp8_f32 v40, v26, v27 op_sel:[0,0,1]
	v_cvt_pk_fp8_f32 v41, v30, v31 op_sel:[0,0,1]
	v_cvt_pk_fp8_f32 v42, v34, v35 op_sel:[0,0,1]
	v_cvt_pk_fp8_f32 v43, v38, v39 op_sel:[0,0,1]
	s_nop 1
	v_permlane32_swap_b32_e32 v40, v42
	v_permlane32_swap_b32_e32 v41, v43
	s_nop 1
	v_permlane16_swap_b32_e32 v40, v41
	v_permlane16_swap_b32_e32 v42, v43
	global_store_dwordx4 v[228:229], v[40:43], off
	v_pk_add_f32 v[24:25], v[76:77], v[4:5]
	v_pk_add_f32 v[26:27], v[78:79], v[6:7]
	v_pk_add_f32 v[28:29], v[68:69], v[4:5]
	v_pk_add_f32 v[30:31], v[70:71], v[6:7]
	v_pk_add_f32 v[32:33], v[72:73], v[0:1]
	v_pk_add_f32 v[34:35], v[74:75], v[2:3]
	v_pk_add_f32 v[36:37], v[64:65], v[0:1]
	v_pk_add_f32 v[38:39], v[66:67], v[2:3]
	v_med3_f32 v24, v24, s77, v200
	v_med3_f32 v25, v25, s77, v200
	v_med3_f32 v26, v26, s77, v200
	v_med3_f32 v27, v27, s77, v200
	v_med3_f32 v28, v28, s77, v200
	v_med3_f32 v29, v29, s77, v200
	v_med3_f32 v30, v30, s77, v200
	v_med3_f32 v31, v31, s77, v200
	v_med3_f32 v32, v32, s77, v200
	v_med3_f32 v33, v33, s77, v200
	v_med3_f32 v34, v34, s77, v200
	v_med3_f32 v35, v35, s77, v200
	v_med3_f32 v36, v36, s77, v200
	v_med3_f32 v37, v37, s77, v200
	v_med3_f32 v38, v38, s77, v200
	v_med3_f32 v39, v39, s77, v200
	v_cvt_pk_fp8_f32 v20, v24, v25
	v_cvt_pk_fp8_f32 v21, v28, v29
	v_cvt_pk_fp8_f32 v22, v32, v33
	v_cvt_pk_fp8_f32 v23, v36, v37
	v_cvt_pk_fp8_f32 v20, v26, v27 op_sel:[0,0,1]
	v_cvt_pk_fp8_f32 v21, v30, v31 op_sel:[0,0,1]
	v_cvt_pk_fp8_f32 v22, v34, v35 op_sel:[0,0,1]
	v_cvt_pk_fp8_f32 v23, v38, v39 op_sel:[0,0,1]
	s_nop 1
	v_permlane32_swap_b32_e32 v20, v22
	v_permlane32_swap_b32_e32 v21, v23
	s_nop 1
	v_permlane16_swap_b32_e32 v20, v21
	v_permlane16_swap_b32_e32 v22, v23
	global_store_dwordx4 v[226:227], v[20:23], off offset:128
	v_pk_add_f32 v[24:25], v[60:61], v[4:5]
	v_pk_add_f32 v[26:27], v[62:63], v[6:7]
	v_pk_add_f32 v[28:29], v[52:53], v[4:5]
	v_pk_add_f32 v[30:31], v[54:55], v[6:7]
	v_pk_add_f32 v[32:33], v[56:57], v[0:1]
	v_pk_add_f32 v[34:35], v[58:59], v[2:3]
	v_pk_add_f32 v[36:37], v[48:49], v[0:1]
	v_pk_add_f32 v[38:39], v[50:51], v[2:3]
	v_med3_f32 v24, v24, s77, v200
	v_med3_f32 v25, v25, s77, v200
	v_med3_f32 v26, v26, s77, v200
	v_med3_f32 v27, v27, s77, v200
	v_med3_f32 v28, v28, s77, v200
	v_med3_f32 v29, v29, s77, v200
	v_med3_f32 v30, v30, s77, v200
	v_med3_f32 v31, v31, s77, v200
	v_med3_f32 v32, v32, s77, v200
	v_med3_f32 v33, v33, s77, v200
	v_med3_f32 v34, v34, s77, v200
	v_med3_f32 v35, v35, s77, v200
	v_med3_f32 v36, v36, s77, v200
	v_med3_f32 v37, v37, s77, v200
	v_med3_f32 v38, v38, s77, v200
	v_med3_f32 v39, v39, s77, v200
	v_cvt_pk_fp8_f32 v40, v24, v25
	v_cvt_pk_fp8_f32 v41, v28, v29
	v_cvt_pk_fp8_f32 v42, v32, v33
	v_cvt_pk_fp8_f32 v43, v36, v37
	v_cvt_pk_fp8_f32 v40, v26, v27 op_sel:[0,0,1]
	v_cvt_pk_fp8_f32 v41, v30, v31 op_sel:[0,0,1]
	v_cvt_pk_fp8_f32 v42, v34, v35 op_sel:[0,0,1]
	v_cvt_pk_fp8_f32 v43, v38, v39 op_sel:[0,0,1]
	s_nop 1
	v_permlane32_swap_b32_e32 v40, v42
	v_permlane32_swap_b32_e32 v41, v43
	s_nop 1
	v_permlane16_swap_b32_e32 v40, v41
	v_permlane16_swap_b32_e32 v42, v43
	global_store_dwordx4 v[228:229], v[40:43], off offset:128
	s_cbranch_vccnz .LBB0_994
	v_mov_b32_e32 v48, 0
	s_mov_b32 s81, s79
	s_mov_b64 s[8:9], s[22:23]
	s_mov_b32 s6, s20
	s_mov_b32 s44, s82
	s_mov_b32 s10, s21
	s_mov_b32 s80, s71
	v_mov_b32_e32 v49, v48
	v_mov_b32_e32 v50, v48
	v_mov_b32_e32 v51, v48
	v_mov_b32_e32 v52, v48
	v_mov_b32_e32 v53, v48
	v_mov_b32_e32 v54, v48
	v_mov_b32_e32 v55, v48
	v_mov_b32_e32 v56, v48
	v_mov_b32_e32 v57, v48
	v_mov_b32_e32 v58, v48
	v_mov_b32_e32 v59, v48
	v_mov_b32_e32 v60, v48
	v_mov_b32_e32 v61, v48
	v_mov_b32_e32 v62, v48
	v_mov_b32_e32 v63, v48
	v_mov_b32_e32 v64, v48
	v_mov_b32_e32 v65, v48
	v_mov_b32_e32 v66, v48
	v_mov_b32_e32 v67, v48
	v_mov_b32_e32 v68, v48
	v_mov_b32_e32 v69, v48
	v_mov_b32_e32 v70, v48
	v_mov_b32_e32 v71, v48
	v_mov_b32_e32 v72, v48
	v_mov_b32_e32 v73, v48
	v_mov_b32_e32 v74, v48
	v_mov_b32_e32 v75, v48
	v_mov_b32_e32 v76, v48
	v_mov_b32_e32 v77, v48
	v_mov_b32_e32 v78, v48
	v_mov_b32_e32 v79, v48
	v_mov_b32_e32 v80, v48
	v_mov_b32_e32 v81, v48
	v_mov_b32_e32 v82, v48
	v_mov_b32_e32 v83, v48
	v_mov_b32_e32 v84, v48
	v_mov_b32_e32 v85, v48
	v_mov_b32_e32 v86, v48
	v_mov_b32_e32 v87, v48
	v_mov_b32_e32 v88, v48
	v_mov_b32_e32 v89, v48
	v_mov_b32_e32 v90, v48
	v_mov_b32_e32 v91, v48
	v_mov_b32_e32 v92, v48
	v_mov_b32_e32 v93, v48
	v_mov_b32_e32 v94, v48
	v_mov_b32_e32 v95, v48
	v_mov_b32_e32 v96, v48
	v_mov_b32_e32 v97, v48
	v_mov_b32_e32 v98, v48
	v_mov_b32_e32 v99, v48
	v_mov_b32_e32 v100, v48
	v_mov_b32_e32 v101, v48
	v_mov_b32_e32 v102, v48
	v_mov_b32_e32 v103, v48
	v_mov_b32_e32 v104, v48
	v_mov_b32_e32 v105, v48
	v_mov_b32_e32 v106, v48
	v_mov_b32_e32 v107, v48
	v_mov_b32_e32 v108, v48
	v_mov_b32_e32 v109, v48
	v_mov_b32_e32 v110, v48
	v_mov_b32_e32 v111, v48
	v_mov_b32_e32 v112, v48
	v_mov_b32_e32 v113, v48
	v_mov_b32_e32 v114, v48
	v_mov_b32_e32 v115, v48
	v_mov_b32_e32 v116, v48
	v_mov_b32_e32 v117, v48
	v_mov_b32_e32 v118, v48
	v_mov_b32_e32 v119, v48
	v_mov_b32_e32 v120, v48
	v_mov_b32_e32 v121, v48
	v_mov_b32_e32 v122, v48
	v_mov_b32_e32 v123, v48
	v_mov_b32_e32 v124, v48
	v_mov_b32_e32 v125, v48
	v_mov_b32_e32 v126, v48
	v_mov_b32_e32 v127, v48
	v_mov_b32_e32 v128, v48
	v_mov_b32_e32 v129, v48
	v_mov_b32_e32 v130, v48
	v_mov_b32_e32 v131, v48
	v_mov_b32_e32 v132, v48
	v_mov_b32_e32 v133, v48
	v_mov_b32_e32 v134, v48
	v_mov_b32_e32 v135, v48
	v_mov_b32_e32 v136, v48
	v_mov_b32_e32 v137, v48
	v_mov_b32_e32 v138, v48
	v_mov_b32_e32 v139, v48
	v_mov_b32_e32 v140, v48
	v_mov_b32_e32 v141, v48
	v_mov_b32_e32 v142, v48
	v_mov_b32_e32 v143, v48
	v_mov_b32_e32 v144, v48
	v_mov_b32_e32 v145, v48
	v_mov_b32_e32 v146, v48
	v_mov_b32_e32 v147, v48
	v_mov_b32_e32 v148, v48
	v_mov_b32_e32 v149, v48
	v_mov_b32_e32 v150, v48
	v_mov_b32_e32 v151, v48
	v_mov_b32_e32 v152, v48
	v_mov_b32_e32 v153, v48
	v_mov_b32_e32 v154, v48
	v_mov_b32_e32 v155, v48
	v_mov_b32_e32 v156, v48
	v_mov_b32_e32 v157, v48
	v_mov_b32_e32 v158, v48
	v_mov_b32_e32 v159, v48
	v_mov_b32_e32 v160, v48
	v_mov_b32_e32 v161, v48
	v_mov_b32_e32 v162, v48
	v_mov_b32_e32 v163, v48
	v_mov_b32_e32 v164, v48
	v_mov_b32_e32 v165, v48
	v_mov_b32_e32 v166, v48
	v_mov_b32_e32 v167, v48
	v_mov_b32_e32 v168, v48
	v_mov_b32_e32 v169, v48
	v_mov_b32_e32 v170, v48
	v_mov_b32_e32 v171, v48
	v_mov_b32_e32 v172, v48
	v_mov_b32_e32 v173, v48
	v_mov_b32_e32 v174, v48
	v_mov_b32_e32 v175, v48
	s_branch .LBB0_994
